# v7 + QKV epilogue (P6): rope cos/sin + act-scale loads prefetched two row-groups ahead in rotating register sets; V path act-scale loads hoisted
# speedup vs baseline: 1.0031x; 1.0031x over previous
.LBB0_712:
	v_add_u32_e32 v100, s48, v178
	v_and_b32_e32 v96, 0xfcf, v176
	v_lshl_add_u64 v[98:99], v[176:177], 2, s[82:83]
	v_ashrrev_i32_e32 v101, 31, v100
	v_lshlrev_b32_e32 v152, 8, v96
	v_lshlrev_b64 v[96:97], 2, v[100:101]
	v_add_u32_e32 v252, v152, v96
	global_load_dword v250, v[98:99], off
	global_load_dwordx4 v[186:189], v252, s[10:11]
	global_load_dwordx4 v[190:193], v252, s[10:11] offset:16
	global_load_dwordx4 v[194:197], v252, s[8:9]
	global_load_dwordx4 v[198:201], v252, s[8:9] offset:16
	v_add_u32_e32 v252, 0x1000, v252
	global_load_dword v251, v[98:99], off offset:64
	global_load_dwordx4 v[234:237], v252, s[10:11]
	global_load_dwordx4 v[238:241], v252, s[10:11] offset:16
	global_load_dwordx4 v[242:245], v252, s[8:9]
	global_load_dwordx4 v[246:249], v252, s[8:9] offset:16
	s_waitcnt vmcnt(5)
	v_mov_b32_e32 v202, v250
	s_cmp_gt_i32 s24, 7
	s_cselect_b32 s19, s56, 0x5ca00000
	s_add_u32 s26, s66, s19
	s_addc_u32 s27, s67, 0
	s_lshl_b32 s19, s24, 1
	s_ashr_i32 s25, s17, 8
	s_and_b32 s19, s19, 14
	s_and_b32 s25, s25, -16
	s_or_b32 s19, s19, s47
	v_lshl_add_u64 v[100:101], v[100:101], 1, s[26:27]
	s_or_b32 s26, s19, s25
	s_ashr_i32 s27, s26, 31
	s_lshl_b64 s[26:27], s[26:27], 20
	v_lshl_add_u64 v[102:103], v[100:101], 0, s[26:27]
	v_lshl_add_u64 v[206:207], v[102:103], 0, v[152:153]
	v_bitop3_b32 v152, v176, s57, 16 bitop3:0xc8
	v_lshlrev_b32_e32 v152, 8, v152
	v_pk_mul_f32 v[208:209], v[58:59], v[202:203] op_sel_hi:[1,0]
	v_pk_mul_f32 v[210:211], v[56:57], v[202:203] op_sel_hi:[1,0]
	v_pk_mul_f32 v[212:213], v[50:51], v[202:203] op_sel_hi:[1,0]
	v_pk_mul_f32 v[214:215], v[48:49], v[202:203] op_sel_hi:[1,0]
	v_pk_mul_f32 v[216:217], v[62:63], v[202:203] op_sel_hi:[1,0]
	v_pk_mul_f32 v[218:219], v[60:61], v[202:203] op_sel_hi:[1,0]
	v_pk_mul_f32 v[220:221], v[54:55], v[202:203] op_sel_hi:[1,0]
	v_pk_mul_f32 v[202:203], v[52:53], v[202:203] op_sel_hi:[1,0]
	v_pk_mul_f32 v[216:217], v[216:217], v[170:171]
	v_pk_mul_f32 v[218:219], v[218:219], v[136:137]
	v_pk_mul_f32 v[220:221], v[220:221], v[174:175]
	v_pk_mul_f32 v[202:203], v[202:203], v[172:173]
	v_pk_mul_f32 v[210:211], v[210:211], v[140:141]
	v_pk_mul_f32 v[208:209], v[208:209], v[142:143]
	v_pk_mul_f32 v[214:215], v[214:215], v[168:169]
	v_pk_mul_f32 v[212:213], v[212:213], v[138:139]
	v_add_u32_e32 v252, 0x1000, v252
	global_load_dword v253, v[98:99], off offset:128
	global_load_dwordx4 v[136:139], v252, s[10:11]
	global_load_dwordx4 v[140:143], v252, s[10:11] offset:16
	global_load_dwordx4 v[168:171], v252, s[8:9]
	global_load_dwordx4 v[172:175], v252, s[8:9] offset:16
	v_pk_mul_f32 v[222:223], v[186:187], v[218:219]
	v_pk_mul_f32 v[224:225], v[188:189], v[216:217]
	v_pk_mul_f32 v[226:227], v[190:191], v[202:203]
	v_pk_mul_f32 v[228:229], v[192:193], v[220:221]
	v_pk_mul_f32 v[218:219], v[194:195], v[218:219]
	v_pk_mul_f32 v[216:217], v[196:197], v[216:217]
	v_pk_mul_f32 v[202:203], v[198:199], v[202:203]
	v_pk_mul_f32 v[220:221], v[200:201], v[220:221]
	v_pk_fma_f32 v[196:197], v[196:197], v[208:209], v[224:225] neg_lo:[0,0,1] neg_hi:[0,0,1]
	v_pk_fma_f32 v[194:195], v[194:195], v[210:211], v[222:223] neg_lo:[0,0,1] neg_hi:[0,0,1]
	v_pk_fma_f32 v[200:201], v[200:201], v[212:213], v[228:229] neg_lo:[0,0,1] neg_hi:[0,0,1]
	v_pk_fma_f32 v[198:199], v[198:199], v[214:215], v[226:227] neg_lo:[0,0,1] neg_hi:[0,0,1]
	v_pk_fma_f32 v[208:209], v[188:189], v[208:209], v[216:217]
	v_pk_fma_f32 v[210:211], v[186:187], v[210:211], v[218:219]
	v_cvt_pk_bf16_f32 v186, v194, v195
	v_cvt_pk_bf16_f32 v187, v196, v197
	v_cvt_pk_bf16_f32 v188, v198, v199
	v_cvt_pk_bf16_f32 v189, v200, v201
	v_pk_fma_f32 v[192:193], v[192:193], v[212:213], v[220:221]
	v_pk_fma_f32 v[190:191], v[190:191], v[214:215], v[202:203]
	global_store_dwordx4 v[206:207], v[186:189], off
	s_nop 1
	v_cvt_pk_bf16_f32 v186, v210, v211
	v_cvt_pk_bf16_f32 v187, v208, v209
	v_cvt_pk_bf16_f32 v188, v190, v191
	v_cvt_pk_bf16_f32 v189, v192, v193
	global_store_dwordx4 v[206:207], v[186:189], off offset:128
	v_add_u32_e32 v252, 0x1000, v252
	global_load_dword v250, v[98:99], off offset:192
	global_load_dwordx4 v[186:189], v252, s[10:11]
	global_load_dwordx4 v[190:193], v252, s[10:11] offset:16
	global_load_dwordx4 v[194:197], v252, s[8:9]
	global_load_dwordx4 v[198:201], v252, s[8:9] offset:16
	s_waitcnt vmcnt(12)
	v_mov_b32_e32 v202, v251
	v_lshl_add_u64 v[206:207], v[102:103], 0, v[152:153]
	v_bitop3_b32 v152, v176, s58, 32 bitop3:0xc8
	v_lshlrev_b32_e32 v152, 8, v152
	v_pk_mul_f32 v[208:209], v[58:59], v[202:203] op_sel_hi:[1,0]
	v_pk_mul_f32 v[210:211], v[56:57], v[202:203] op_sel_hi:[1,0]
	v_pk_mul_f32 v[212:213], v[50:51], v[202:203] op_sel_hi:[1,0]
	v_pk_mul_f32 v[214:215], v[48:49], v[202:203] op_sel_hi:[1,0]
	v_pk_mul_f32 v[216:217], v[62:63], v[202:203] op_sel_hi:[1,0]
	v_pk_mul_f32 v[218:219], v[60:61], v[202:203] op_sel_hi:[1,0]
	v_pk_mul_f32 v[220:221], v[54:55], v[202:203] op_sel_hi:[1,0]
	v_pk_mul_f32 v[202:203], v[52:53], v[202:203] op_sel_hi:[1,0]
	v_pk_mul_f32 v[218:219], v[218:219], v[130:131]
	v_pk_mul_f32 v[216:217], v[216:217], v[128:129]
	v_pk_mul_f32 v[202:203], v[202:203], v[134:135]
	v_pk_mul_f32 v[220:221], v[220:221], v[132:133]
	v_pk_mul_f32 v[210:211], v[210:211], v[122:123]
	v_pk_mul_f32 v[208:209], v[208:209], v[120:121]
	v_pk_mul_f32 v[214:215], v[214:215], v[126:127]
	v_pk_mul_f32 v[212:213], v[212:213], v[124:125]
	v_pk_mul_f32 v[222:223], v[236:237], v[216:217]
	v_pk_mul_f32 v[224:225], v[234:235], v[218:219]
	v_pk_mul_f32 v[226:227], v[240:241], v[220:221]
	v_pk_mul_f32 v[228:229], v[238:239], v[202:203]
	v_pk_mul_f32 v[216:217], v[244:245], v[216:217]
	v_pk_mul_f32 v[218:219], v[242:243], v[218:219]
	v_pk_mul_f32 v[220:221], v[248:249], v[220:221]
	v_pk_mul_f32 v[202:203], v[246:247], v[202:203]
	v_pk_fma_f32 v[244:245], v[244:245], v[208:209], v[222:223] neg_lo:[0,0,1] neg_hi:[0,0,1]
	v_pk_fma_f32 v[242:243], v[242:243], v[210:211], v[224:225] neg_lo:[0,0,1] neg_hi:[0,0,1]
	v_pk_fma_f32 v[248:249], v[248:249], v[212:213], v[226:227] neg_lo:[0,0,1] neg_hi:[0,0,1]
	v_pk_fma_f32 v[246:247], v[246:247], v[214:215], v[228:229] neg_lo:[0,0,1] neg_hi:[0,0,1]
	v_pk_fma_f32 v[208:209], v[236:237], v[208:209], v[216:217]
	v_pk_fma_f32 v[210:211], v[234:235], v[210:211], v[218:219]
	v_cvt_pk_bf16_f32 v234, v242, v243
	v_cvt_pk_bf16_f32 v235, v244, v245
	v_cvt_pk_bf16_f32 v236, v246, v247
	v_cvt_pk_bf16_f32 v237, v248, v249
	v_pk_fma_f32 v[240:241], v[240:241], v[212:213], v[220:221]
	v_pk_fma_f32 v[238:239], v[238:239], v[214:215], v[202:203]
	global_store_dwordx4 v[206:207], v[234:237], off
	s_nop 1
	v_cvt_pk_bf16_f32 v234, v210, v211
	v_cvt_pk_bf16_f32 v235, v208, v209
	v_cvt_pk_bf16_f32 v236, v238, v239
	v_cvt_pk_bf16_f32 v237, v240, v241
	global_store_dwordx4 v[206:207], v[234:237], off offset:128
	v_add_u32_e32 v252, 0x5000, v252
	global_load_dword v251, v[98:99], off offset:512
	global_load_dwordx4 v[234:237], v252, s[10:11]
	global_load_dwordx4 v[238:241], v252, s[10:11] offset:16
	global_load_dwordx4 v[242:245], v252, s[8:9]
	global_load_dwordx4 v[246:249], v252, s[8:9] offset:16
	s_waitcnt vmcnt(14)
	v_mov_b32_e32 v202, v253
	v_lshl_add_u64 v[206:207], v[102:103], 0, v[152:153]
	v_bitop3_b32 v152, v176, s59, 48 bitop3:0xc8
	v_lshlrev_b32_e32 v152, 8, v152
	v_lshl_add_u64 v[102:103], v[102:103], 0, v[152:153]
	v_pk_mul_f32 v[208:209], v[58:59], v[202:203] op_sel_hi:[1,0]
	v_pk_mul_f32 v[210:211], v[56:57], v[202:203] op_sel_hi:[1,0]
	v_pk_mul_f32 v[212:213], v[50:51], v[202:203] op_sel_hi:[1,0]
	v_pk_mul_f32 v[214:215], v[48:49], v[202:203] op_sel_hi:[1,0]
	v_pk_mul_f32 v[216:217], v[62:63], v[202:203] op_sel_hi:[1,0]
	v_pk_mul_f32 v[218:219], v[60:61], v[202:203] op_sel_hi:[1,0]
	v_pk_mul_f32 v[220:221], v[54:55], v[202:203] op_sel_hi:[1,0]
	v_pk_mul_f32 v[202:203], v[52:53], v[202:203] op_sel_hi:[1,0]
	v_pk_mul_f32 v[218:219], v[218:219], v[116:117]
	v_pk_mul_f32 v[216:217], v[216:217], v[110:111]
	v_pk_mul_f32 v[202:203], v[202:203], v[118:119]
	v_pk_mul_f32 v[220:221], v[220:221], v[114:115]
	v_pk_mul_f32 v[210:211], v[210:211], v[108:109]
	v_pk_mul_f32 v[208:209], v[208:209], v[104:105]
	v_pk_mul_f32 v[214:215], v[214:215], v[112:113]
	v_pk_mul_f32 v[212:213], v[212:213], v[106:107]
	v_pk_mul_f32 v[222:223], v[138:139], v[216:217]
	v_pk_mul_f32 v[224:225], v[136:137], v[218:219]
	v_pk_mul_f32 v[226:227], v[142:143], v[220:221]
	v_pk_mul_f32 v[228:229], v[140:141], v[202:203]
	v_pk_mul_f32 v[216:217], v[170:171], v[216:217]
	v_pk_mul_f32 v[218:219], v[168:169], v[218:219]
	v_pk_mul_f32 v[220:221], v[174:175], v[220:221]
	v_pk_mul_f32 v[202:203], v[172:173], v[202:203]
	v_pk_fma_f32 v[170:171], v[170:171], v[208:209], v[222:223] neg_lo:[0,0,1] neg_hi:[0,0,1]
	v_pk_fma_f32 v[168:169], v[168:169], v[210:211], v[224:225] neg_lo:[0,0,1] neg_hi:[0,0,1]
	v_pk_fma_f32 v[174:175], v[174:175], v[212:213], v[226:227] neg_lo:[0,0,1] neg_hi:[0,0,1]
	v_pk_fma_f32 v[172:173], v[172:173], v[214:215], v[228:229] neg_lo:[0,0,1] neg_hi:[0,0,1]
	v_pk_fma_f32 v[208:209], v[138:139], v[208:209], v[216:217]
	v_pk_fma_f32 v[210:211], v[136:137], v[210:211], v[218:219]
	v_cvt_pk_bf16_f32 v136, v168, v169
	v_cvt_pk_bf16_f32 v137, v170, v171
	v_cvt_pk_bf16_f32 v138, v172, v173
	v_cvt_pk_bf16_f32 v139, v174, v175
	v_pk_fma_f32 v[142:143], v[142:143], v[212:213], v[220:221]
	v_pk_fma_f32 v[140:141], v[140:141], v[214:215], v[202:203]
	global_store_dwordx4 v[206:207], v[136:139], off
	s_nop 1
	v_cvt_pk_bf16_f32 v136, v210, v211
	v_cvt_pk_bf16_f32 v137, v208, v209
	v_cvt_pk_bf16_f32 v138, v140, v141
	v_cvt_pk_bf16_f32 v139, v142, v143
	global_store_dwordx4 v[206:207], v[136:139], off offset:128
	v_add_u32_e32 v252, 0x1000, v252
	global_load_dword v253, v[98:99], off offset:576
	global_load_dwordx4 v[136:139], v252, s[10:11]
	global_load_dwordx4 v[140:143], v252, s[10:11] offset:16
	global_load_dwordx4 v[168:171], v252, s[8:9]
	global_load_dwordx4 v[172:175], v252, s[8:9] offset:16
	s_waitcnt vmcnt(14)
	v_mov_b32_e32 v202, v250
	v_pk_mul_f32 v[204:205], v[58:59], v[202:203] op_sel_hi:[1,0]
	v_pk_mul_f32 v[206:207], v[56:57], v[202:203] op_sel_hi:[1,0]
	v_pk_mul_f32 v[208:209], v[50:51], v[202:203] op_sel_hi:[1,0]
	v_pk_mul_f32 v[210:211], v[48:49], v[202:203] op_sel_hi:[1,0]
	v_pk_mul_f32 v[212:213], v[62:63], v[202:203] op_sel_hi:[1,0]
	v_pk_mul_f32 v[214:215], v[60:61], v[202:203] op_sel_hi:[1,0]
	v_pk_mul_f32 v[216:217], v[54:55], v[202:203] op_sel_hi:[1,0]
	v_pk_mul_f32 v[202:203], v[52:53], v[202:203] op_sel_hi:[1,0]
	v_pk_mul_f32 v[214:215], v[214:215], v[84:85]
	v_pk_mul_f32 v[212:213], v[212:213], v[86:87]
	v_pk_mul_f32 v[202:203], v[202:203], v[80:81]
	v_pk_mul_f32 v[216:217], v[216:217], v[82:83]
	v_pk_mul_f32 v[206:207], v[206:207], v[90:91]
	v_pk_mul_f32 v[204:205], v[204:205], v[88:89]
	v_pk_mul_f32 v[210:211], v[210:211], v[94:95]
	v_pk_mul_f32 v[208:209], v[208:209], v[92:93]
	v_pk_mul_f32 v[218:219], v[188:189], v[212:213]
	v_pk_mul_f32 v[220:221], v[186:187], v[214:215]
	v_pk_mul_f32 v[222:223], v[192:193], v[216:217]
	v_pk_mul_f32 v[224:225], v[190:191], v[202:203]
	v_pk_mul_f32 v[212:213], v[196:197], v[212:213]
	v_pk_mul_f32 v[214:215], v[194:195], v[214:215]
	v_pk_mul_f32 v[216:217], v[200:201], v[216:217]
	v_pk_mul_f32 v[202:203], v[198:199], v[202:203]
	v_pk_fma_f32 v[196:197], v[196:197], v[204:205], v[218:219] neg_lo:[0,0,1] neg_hi:[0,0,1]
	v_pk_fma_f32 v[194:195], v[194:195], v[206:207], v[220:221] neg_lo:[0,0,1] neg_hi:[0,0,1]
	v_pk_fma_f32 v[200:201], v[200:201], v[208:209], v[222:223] neg_lo:[0,0,1] neg_hi:[0,0,1]
	v_pk_fma_f32 v[198:199], v[198:199], v[210:211], v[224:225] neg_lo:[0,0,1] neg_hi:[0,0,1]
	v_pk_fma_f32 v[204:205], v[188:189], v[204:205], v[212:213]
	v_pk_fma_f32 v[206:207], v[186:187], v[206:207], v[214:215]
	v_cvt_pk_bf16_f32 v186, v194, v195
	v_cvt_pk_bf16_f32 v187, v196, v197
	v_cvt_pk_bf16_f32 v188, v198, v199
	v_cvt_pk_bf16_f32 v189, v200, v201
	v_pk_fma_f32 v[192:193], v[192:193], v[208:209], v[216:217]
	v_pk_fma_f32 v[190:191], v[190:191], v[210:211], v[202:203]
	global_store_dwordx4 v[102:103], v[186:189], off
	s_nop 1
	v_cvt_pk_bf16_f32 v186, v206, v207
	v_cvt_pk_bf16_f32 v187, v204, v205
	v_cvt_pk_bf16_f32 v188, v190, v191
	v_cvt_pk_bf16_f32 v189, v192, v193
	global_store_dwordx4 v[102:103], v[186:189], off offset:128
	v_add_u32_e32 v252, 0x1000, v252
	global_load_dword v250, v[98:99], off offset:640
	global_load_dwordx4 v[186:189], v252, s[10:11]
	global_load_dwordx4 v[190:193], v252, s[10:11] offset:16
	global_load_dwordx4 v[194:197], v252, s[8:9]
	global_load_dwordx4 v[198:201], v252, s[8:9] offset:16
	v_and_b32_e32 v103, 0xfcf, v179
	v_lshlrev_b32_e32 v152, 8, v103
	s_waitcnt vmcnt(14)
	v_mov_b32_e32 v102, v251
	v_ashrrev_i32_e32 v103, 8, v179
	v_and_or_b32 v202, v103, -16, s19
	v_ashrrev_i32_e32 v203, 31, v202
	v_lshlrev_b64 v[202:203], 20, v[202:203]
	v_lshl_add_u64 v[100:101], v[100:101], 0, v[202:203]
	v_lshl_add_u64 v[202:203], v[100:101], 0, v[152:153]
	v_pk_mul_f32 v[204:205], v[58:59], v[102:103] op_sel_hi:[1,0]
	v_pk_mul_f32 v[206:207], v[56:57], v[102:103] op_sel_hi:[1,0]
	v_pk_mul_f32 v[208:209], v[50:51], v[102:103] op_sel_hi:[1,0]
	v_pk_mul_f32 v[210:211], v[48:49], v[102:103] op_sel_hi:[1,0]
	v_pk_mul_f32 v[212:213], v[62:63], v[102:103] op_sel_hi:[1,0]
	v_pk_mul_f32 v[214:215], v[60:61], v[102:103] op_sel_hi:[1,0]
	v_pk_mul_f32 v[216:217], v[54:55], v[102:103] op_sel_hi:[1,0]
	v_pk_mul_f32 v[102:103], v[52:53], v[102:103] op_sel_hi:[1,0]
	v_pk_mul_f32 v[212:213], v[212:213], v[70:71]
	v_pk_mul_f32 v[214:215], v[214:215], v[68:69]
	v_pk_mul_f32 v[102:103], v[102:103], v[64:65]
	v_pk_mul_f32 v[206:207], v[206:207], v[76:77]
	v_pk_mul_f32 v[204:205], v[204:205], v[78:79]
	v_pk_mul_f32 v[210:211], v[210:211], v[72:73]
	v_pk_mul_f32 v[216:217], v[216:217], v[66:67]
	v_pk_mul_f32 v[218:219], v[234:235], v[214:215]
	v_pk_mul_f32 v[220:221], v[236:237], v[212:213]
	v_pk_mul_f32 v[222:223], v[238:239], v[102:103]
	v_pk_mul_f32 v[214:215], v[242:243], v[214:215]
	v_pk_mul_f32 v[212:213], v[244:245], v[212:213]
	v_pk_mul_f32 v[102:103], v[246:247], v[102:103]
	v_pk_mul_f32 v[208:209], v[208:209], v[74:75]
	v_pk_mul_f32 v[224:225], v[240:241], v[216:217]
	v_pk_fma_f32 v[244:245], v[244:245], v[204:205], v[220:221] neg_lo:[0,0,1] neg_hi:[0,0,1]
	v_pk_fma_f32 v[242:243], v[242:243], v[206:207], v[218:219] neg_lo:[0,0,1] neg_hi:[0,0,1]
	v_pk_fma_f32 v[246:247], v[246:247], v[210:211], v[222:223] neg_lo:[0,0,1] neg_hi:[0,0,1]
	v_pk_fma_f32 v[204:205], v[236:237], v[204:205], v[212:213]
	v_pk_fma_f32 v[206:207], v[234:235], v[206:207], v[214:215]
	v_pk_fma_f32 v[102:103], v[238:239], v[210:211], v[102:103]
	v_cvt_pk_bf16_f32 v234, v242, v243
	v_cvt_pk_bf16_f32 v235, v244, v245
	v_cvt_pk_bf16_f32 v236, v246, v247
	v_pk_mul_f32 v[216:217], v[248:249], v[216:217]
	v_pk_fma_f32 v[248:249], v[248:249], v[208:209], v[224:225] neg_lo:[0,0,1] neg_hi:[0,0,1]
	v_pk_fma_f32 v[240:241], v[240:241], v[208:209], v[216:217]
	v_cvt_pk_bf16_f32 v237, v248, v249
	global_store_dwordx4 v[202:203], v[234:237], off
	s_nop 1
	v_cvt_f32_i32_e32 v211, v37
	v_cvt_f32_i32_e32 v210, v36
	v_cvt_pk_bf16_f32 v234, v206, v207
	v_cvt_pk_bf16_f32 v235, v204, v205
	v_cvt_pk_bf16_f32 v236, v102, v103
	v_add_u32_e32 v103, 0x90, v176
	v_and_b32_e32 v103, 0xfdf, v103
	v_cvt_pk_bf16_f32 v237, v240, v241
	global_store_dwordx4 v[202:203], v[234:237], off offset:128
	v_add_u32_e32 v252, 0x1000, v252
	global_load_dword v251, v[98:99], off offset:704
	global_load_dwordx4 v[234:237], v252, s[10:11]
	global_load_dwordx4 v[238:241], v252, s[10:11] offset:16
	global_load_dwordx4 v[120:123], v252, s[8:9]
	global_load_dwordx4 v[242:245], v252, s[8:9] offset:16
	v_lshlrev_b32_e32 v152, 8, v103
	s_waitcnt vmcnt(14)
	v_mov_b32_e32 v102, v253
	v_cvt_f32_i32_e32 v213, v39
	v_cvt_f32_i32_e32 v212, v38
	v_cvt_f32_i32_e32 v215, v33
	v_cvt_f32_i32_e32 v214, v32
	v_cvt_f32_i32_e32 v203, v47
	v_cvt_f32_i32_e32 v202, v46
	v_cvt_f32_i32_e32 v205, v45
	v_cvt_f32_i32_e32 v204, v44
	v_cvt_f32_i32_e32 v209, v41
	v_cvt_f32_i32_e32 v208, v40
	v_cvt_f32_i32_e32 v217, v35
	v_cvt_f32_i32_e32 v216, v34
	v_cvt_f32_i32_e32 v207, v43
	v_cvt_f32_i32_e32 v206, v42
	v_lshl_add_u64 v[218:219], v[100:101], 0, v[152:153]
	v_pk_mul_f32 v[220:221], v[58:59], v[102:103] op_sel_hi:[1,0]
	v_pk_mul_f32 v[222:223], v[56:57], v[102:103] op_sel_hi:[1,0]
	v_pk_mul_f32 v[224:225], v[50:51], v[102:103] op_sel_hi:[1,0]
	v_pk_mul_f32 v[226:227], v[48:49], v[102:103] op_sel_hi:[1,0]
	v_pk_mul_f32 v[228:229], v[62:63], v[102:103] op_sel_hi:[1,0]
	v_pk_mul_f32 v[230:231], v[60:61], v[102:103] op_sel_hi:[1,0]
	v_pk_mul_f32 v[232:233], v[54:55], v[102:103] op_sel_hi:[1,0]
	v_pk_mul_f32 v[102:103], v[52:53], v[102:103] op_sel_hi:[1,0]
	v_pk_mul_f32 v[212:213], v[228:229], v[212:213]
	v_pk_mul_f32 v[210:211], v[230:231], v[210:211]
	v_pk_mul_f32 v[102:103], v[102:103], v[214:215]
	v_pk_mul_f32 v[204:205], v[222:223], v[204:205]
	v_pk_mul_f32 v[202:203], v[220:221], v[202:203]
	v_pk_mul_f32 v[208:209], v[226:227], v[208:209]
	v_pk_mul_f32 v[216:217], v[232:233], v[216:217]
	v_pk_mul_f32 v[214:215], v[136:137], v[210:211]
	v_pk_mul_f32 v[220:221], v[138:139], v[212:213]
	v_pk_mul_f32 v[222:223], v[140:141], v[102:103]
	v_pk_mul_f32 v[210:211], v[168:169], v[210:211]
	v_pk_mul_f32 v[212:213], v[170:171], v[212:213]
	v_pk_mul_f32 v[102:103], v[172:173], v[102:103]
	v_pk_mul_f32 v[206:207], v[224:225], v[206:207]
	v_pk_mul_f32 v[224:225], v[142:143], v[216:217]
	v_pk_fma_f32 v[170:171], v[170:171], v[202:203], v[220:221] neg_lo:[0,0,1] neg_hi:[0,0,1]
	v_pk_fma_f32 v[168:169], v[168:169], v[204:205], v[214:215] neg_lo:[0,0,1] neg_hi:[0,0,1]
	v_pk_fma_f32 v[172:173], v[172:173], v[208:209], v[222:223] neg_lo:[0,0,1] neg_hi:[0,0,1]
	v_pk_fma_f32 v[202:203], v[138:139], v[202:203], v[212:213]
	v_pk_fma_f32 v[204:205], v[136:137], v[204:205], v[210:211]
	v_pk_fma_f32 v[102:103], v[140:141], v[208:209], v[102:103]
	v_cvt_pk_bf16_f32 v136, v168, v169
	v_cvt_pk_bf16_f32 v137, v170, v171
	v_cvt_pk_bf16_f32 v138, v172, v173
	v_pk_mul_f32 v[216:217], v[174:175], v[216:217]
	v_pk_fma_f32 v[174:175], v[174:175], v[206:207], v[224:225] neg_lo:[0,0,1] neg_hi:[0,0,1]
	v_pk_fma_f32 v[142:143], v[142:143], v[206:207], v[216:217]
	v_cvt_pk_bf16_f32 v139, v174, v175
	global_store_dwordx4 v[218:219], v[136:139], off
	s_nop 1
	v_cvt_f32_i32_e32 v211, v21
	v_cvt_f32_i32_e32 v210, v20
	v_cvt_pk_bf16_f32 v136, v204, v205
	v_cvt_pk_bf16_f32 v137, v202, v203
	v_cvt_pk_bf16_f32 v138, v102, v103
	v_add_u32_e32 v103, 0xa0, v176
	v_and_b32_e32 v103, 0xfef, v103
	v_cvt_pk_bf16_f32 v139, v142, v143
	global_store_dwordx4 v[218:219], v[136:139], off offset:128
	v_lshlrev_b32_e32 v152, 8, v103
	s_waitcnt vmcnt(9)
	v_mov_b32_e32 v102, v250
	v_cvt_f32_i32_e32 v213, v23
	v_cvt_f32_i32_e32 v212, v22
	v_cvt_f32_i32_e32 v215, v17
	v_cvt_f32_i32_e32 v214, v16
	v_cvt_f32_i32_e32 v217, v19
	v_cvt_f32_i32_e32 v216, v18
	v_cvt_f32_i32_e32 v203, v31
	v_cvt_f32_i32_e32 v202, v30
	v_cvt_f32_i32_e32 v205, v29
	v_cvt_f32_i32_e32 v204, v28
	v_cvt_f32_i32_e32 v207, v27
	v_cvt_f32_i32_e32 v206, v26
	v_cvt_f32_i32_e32 v209, v25
	v_cvt_f32_i32_e32 v208, v24
	v_lshl_add_u64 v[218:219], v[100:101], 0, v[152:153]
	v_pk_mul_f32 v[220:221], v[58:59], v[102:103] op_sel_hi:[1,0]
	v_pk_mul_f32 v[222:223], v[56:57], v[102:103] op_sel_hi:[1,0]
	v_pk_mul_f32 v[224:225], v[50:51], v[102:103] op_sel_hi:[1,0]
	v_pk_mul_f32 v[226:227], v[48:49], v[102:103] op_sel_hi:[1,0]
	v_pk_mul_f32 v[228:229], v[62:63], v[102:103] op_sel_hi:[1,0]
	v_pk_mul_f32 v[230:231], v[60:61], v[102:103] op_sel_hi:[1,0]
	v_pk_mul_f32 v[232:233], v[54:55], v[102:103] op_sel_hi:[1,0]
	v_pk_mul_f32 v[102:103], v[52:53], v[102:103] op_sel_hi:[1,0]
	v_pk_mul_f32 v[212:213], v[228:229], v[212:213]
	v_pk_mul_f32 v[210:211], v[230:231], v[210:211]
	v_pk_mul_f32 v[216:217], v[232:233], v[216:217]
	v_pk_mul_f32 v[102:103], v[102:103], v[214:215]
	v_pk_mul_f32 v[204:205], v[222:223], v[204:205]
	v_pk_mul_f32 v[202:203], v[220:221], v[202:203]
	v_pk_mul_f32 v[208:209], v[226:227], v[208:209]
	v_pk_mul_f32 v[206:207], v[224:225], v[206:207]
	v_pk_mul_f32 v[214:215], v[186:187], v[210:211]
	v_pk_mul_f32 v[220:221], v[188:189], v[212:213]
	v_pk_mul_f32 v[222:223], v[190:191], v[102:103]
	v_pk_mul_f32 v[224:225], v[192:193], v[216:217]
	v_pk_mul_f32 v[210:211], v[194:195], v[210:211]
	v_pk_mul_f32 v[212:213], v[196:197], v[212:213]
	v_pk_mul_f32 v[102:103], v[198:199], v[102:103]
	v_pk_mul_f32 v[216:217], v[200:201], v[216:217]
	v_pk_fma_f32 v[196:197], v[196:197], v[202:203], v[220:221] neg_lo:[0,0,1] neg_hi:[0,0,1]
	v_pk_fma_f32 v[194:195], v[194:195], v[204:205], v[214:215] neg_lo:[0,0,1] neg_hi:[0,0,1]
	v_pk_fma_f32 v[200:201], v[200:201], v[206:207], v[224:225] neg_lo:[0,0,1] neg_hi:[0,0,1]
	v_pk_fma_f32 v[198:199], v[198:199], v[208:209], v[222:223] neg_lo:[0,0,1] neg_hi:[0,0,1]
	v_pk_fma_f32 v[202:203], v[188:189], v[202:203], v[212:213]
	v_pk_fma_f32 v[204:205], v[186:187], v[204:205], v[210:211]
	v_cvt_pk_bf16_f32 v186, v194, v195
	v_cvt_pk_bf16_f32 v187, v196, v197
	v_cvt_pk_bf16_f32 v188, v198, v199
	v_cvt_pk_bf16_f32 v189, v200, v201
	v_pk_fma_f32 v[192:193], v[192:193], v[206:207], v[216:217]
	v_pk_fma_f32 v[102:103], v[190:191], v[208:209], v[102:103]
	global_store_dwordx4 v[218:219], v[186:189], off
	s_nop 1
	v_cvt_f32_i32_e32 v207, v5
	v_cvt_f32_i32_e32 v206, v4
	v_cvt_pk_bf16_f32 v186, v204, v205
	v_cvt_pk_bf16_f32 v187, v202, v203
	v_cvt_pk_bf16_f32 v188, v102, v103
	v_cvt_pk_bf16_f32 v189, v192, v193
	global_store_dwordx4 v[218:219], v[186:189], off offset:128
	s_waitcnt vmcnt(4)
	v_mov_b32_e32 v102, v251
	v_add_u32_e32 v98, 0xb0, v176
	v_and_b32_e32 v98, 0xfff, v98
	v_lshlrev_b32_e32 v152, 8, v98
	v_cvt_f32_i32_e32 v209, v7
	v_cvt_f32_i32_e32 v208, v6
	v_cvt_f32_i32_e32 v247, v15
	v_cvt_f32_i32_e32 v246, v14
	v_cvt_f32_i32_e32 v249, v13
	v_cvt_f32_i32_e32 v248, v12
	v_cvt_f32_i32_e32 v211, v1
	v_cvt_f32_i32_e32 v210, v0
	v_cvt_f32_i32_e32 v213, v3
	v_cvt_f32_i32_e32 v212, v2
	v_cvt_f32_i32_e32 v203, v11
	v_cvt_f32_i32_e32 v202, v10
	v_cvt_f32_i32_e32 v205, v9
	v_cvt_f32_i32_e32 v204, v8
	v_lshl_add_u64 v[100:101], v[100:101], 0, v[152:153]
	v_pk_mul_f32 v[222:223], v[62:63], v[102:103] op_sel_hi:[1,0]
	v_pk_mul_f32 v[224:225], v[60:61], v[102:103] op_sel_hi:[1,0]
	v_pk_mul_f32 v[214:215], v[58:59], v[102:103] op_sel_hi:[1,0]
	v_pk_mul_f32 v[216:217], v[56:57], v[102:103] op_sel_hi:[1,0]
	v_pk_mul_f32 v[218:219], v[50:51], v[102:103] op_sel_hi:[1,0]
	v_pk_mul_f32 v[220:221], v[48:49], v[102:103] op_sel_hi:[1,0]
	v_pk_mul_f32 v[226:227], v[54:55], v[102:103] op_sel_hi:[1,0]
	v_pk_mul_f32 v[102:103], v[52:53], v[102:103] op_sel_hi:[1,0]
	v_pk_mul_f32 v[208:209], v[222:223], v[208:209]
	v_pk_mul_f32 v[206:207], v[224:225], v[206:207]
	v_pk_mul_f32 v[248:249], v[216:217], v[248:249]
	v_pk_mul_f32 v[246:247], v[214:215], v[246:247]
	v_pk_mul_f32 v[212:213], v[226:227], v[212:213]
	v_pk_mul_f32 v[102:103], v[102:103], v[210:211]
	v_pk_mul_f32 v[210:211], v[234:235], v[206:207]
	v_pk_mul_f32 v[214:215], v[236:237], v[208:209]
	v_pk_mul_f32 v[204:205], v[220:221], v[204:205]
	v_pk_mul_f32 v[202:203], v[218:219], v[202:203]
	v_pk_mul_f32 v[216:217], v[238:239], v[102:103]
	v_pk_mul_f32 v[218:219], v[240:241], v[212:213]
	v_pk_mul_f32 v[206:207], v[120:121], v[206:207]
	v_pk_mul_f32 v[208:209], v[122:123], v[208:209]
	v_pk_fma_f32 v[122:123], v[122:123], v[246:247], v[214:215] neg_lo:[0,0,1] neg_hi:[0,0,1]
	v_pk_fma_f32 v[120:121], v[120:121], v[248:249], v[210:211] neg_lo:[0,0,1] neg_hi:[0,0,1]
	v_pk_mul_f32 v[102:103], v[242:243], v[102:103]
	v_pk_mul_f32 v[212:213], v[244:245], v[212:213]
	v_pk_fma_f32 v[244:245], v[244:245], v[202:203], v[218:219] neg_lo:[0,0,1] neg_hi:[0,0,1]
	v_pk_fma_f32 v[242:243], v[242:243], v[204:205], v[216:217] neg_lo:[0,0,1] neg_hi:[0,0,1]
	v_cvt_pk_bf16_f32 v120, v120, v121
	v_cvt_pk_bf16_f32 v121, v122, v123
	v_pk_fma_f32 v[236:237], v[236:237], v[246:247], v[208:209]
	v_cvt_pk_bf16_f32 v122, v242, v243
	v_cvt_pk_bf16_f32 v123, v244, v245
	v_pk_fma_f32 v[234:235], v[234:235], v[248:249], v[206:207]
	v_pk_fma_f32 v[240:241], v[240:241], v[202:203], v[212:213]
	v_pk_fma_f32 v[102:103], v[238:239], v[204:205], v[102:103]
	global_store_dwordx4 v[100:101], v[120:123], off
	s_nop 1
	v_cvt_pk_bf16_f32 v120, v234, v235
	v_cvt_pk_bf16_f32 v121, v236, v237
	v_cvt_pk_bf16_f32 v122, v102, v103
	v_cvt_pk_bf16_f32 v123, v240, v241
	global_store_dwordx4 v[100:101], v[120:123], off offset:128
	s_cbranch_execnz .LBB0_711
.LBB0_713:
	s_nop 0
	v_lshl_add_u64 v[98:99], v[176:177], 2, s[82:83]
	global_load_dword v100, v[98:99], off
	global_load_dword v234, v[98:99], off offset:64
	global_load_dword v236, v[98:99], off offset:128
	global_load_dword v238, v[98:99], off offset:192
	global_load_dword v240, v[98:99], off offset:512
	global_load_dword v242, v[98:99], off offset:576
	global_load_dword v244, v[98:99], off offset:640
	global_load_dword v246, v[98:99], off offset:704
	s_lshl_b32 s19, s24, 1
	s_ashr_i32 s24, s17, 8
	s_sub_i32 s17, s19, 32
	s_and_b32 s19, s24, -16
	s_add_i32 s24, s19, s17
	s_ashr_i32 s25, s24, 31
	s_lshl_b64 s[26:27], s[24:25], 20
	s_add_u32 s26, s6, s26
	s_addc_u32 s27, s7, s27
	s_or_b32 s24, s24, 1
	s_ashr_i32 s25, s24, 31
	v_add_u32_e32 v96, s46, v178
	v_lshlrev_b32_e32 v178, 8, v176
	s_lshl_b64 s[24:25], s[24:25], 20
	v_ashrrev_i32_e32 v97, 31, v96
	v_and_b32_e32 v152, 0xfcf00, v178
	s_add_u32 s24, s6, s24
	v_lshlrev_b64 v[96:97], 1, v[96:97]
	v_lshl_add_u64 v[102:103], s[26:27], 0, v[152:153]
	s_addc_u32 s25, s7, s25
	v_lshl_add_u64 v[188:189], v[102:103], 0, v[96:97]
	v_lshl_add_u64 v[102:103], s[24:25], 0, v[152:153]
	v_lshl_add_u64 v[190:191], v[102:103], 0, v[96:97]
	v_lshlrev_b32_e32 v152, 8, v166
	v_and_b32_e32 v152, 0xfdf00, v152
	v_lshl_add_u64 v[166:167], s[26:27], 0, v[152:153]
	v_cvt_f32_i32_e32 v45, v45
	v_cvt_f32_i32_e32 v44, v44
	v_cvt_f32_i32_e32 v47, v47
	v_cvt_f32_i32_e32 v46, v46
	v_cvt_f32_i32_e32 v41, v41
	v_cvt_f32_i32_e32 v40, v40
	v_cvt_f32_i32_e32 v43, v43
	v_cvt_f32_i32_e32 v42, v42
	v_cvt_f32_i32_e32 v39, v39
	v_cvt_f32_i32_e32 v38, v38
	v_cvt_f32_i32_e32 v31, v31
	v_cvt_f32_i32_e32 v30, v30
	v_cvt_f32_i32_e32 v29, v29
	v_cvt_f32_i32_e32 v28, v28
	v_cvt_f32_i32_e32 v27, v27
	v_cvt_f32_i32_e32 v26, v26
	v_cvt_f32_i32_e32 v25, v25
	v_cvt_f32_i32_e32 v24, v24
	v_cvt_f32_i32_e32 v23, v23
	v_cvt_f32_i32_e32 v22, v22
	v_cvt_f32_i32_e32 v21, v21
	v_cvt_f32_i32_e32 v20, v20
	v_cvt_f32_i32_e32 v19, v19
	v_cvt_f32_i32_e32 v18, v18
	v_cvt_f32_i32_e32 v17, v17
	v_cvt_f32_i32_e32 v16, v16
	v_cvt_f32_i32_e32 v15, v15
	v_cvt_f32_i32_e32 v14, v14
	v_cvt_f32_i32_e32 v11, v11
	v_cvt_f32_i32_e32 v10, v10
	v_cvt_f32_i32_e32 v7, v7
	v_cvt_f32_i32_e32 v6, v6
	v_cvt_f32_i32_e32 v13, v13
	v_cvt_f32_i32_e32 v12, v12
	v_cvt_f32_i32_e32 v9, v9
	v_cvt_f32_i32_e32 v8, v8
	v_cvt_f32_i32_e32 v5, v5
	v_cvt_f32_i32_e32 v4, v4
	v_xor_b32_e32 v185, 16, v184
	s_waitcnt vmcnt(0)
	v_pk_mul_f32 v[102:103], v[58:59], v[100:101] op_sel_hi:[1,0]
	v_pk_mul_f32 v[176:177], v[56:57], v[100:101] op_sel_hi:[1,0]
	v_pk_mul_f32 v[192:193], v[50:51], v[100:101] op_sel_hi:[1,0]
	v_pk_mul_f32 v[194:195], v[48:49], v[100:101] op_sel_hi:[1,0]
	v_pk_mul_f32 v[196:197], v[62:63], v[100:101] op_sel_hi:[1,0]
	v_pk_mul_f32 v[202:203], v[52:53], v[100:101] op_sel_hi:[1,0]
	v_pk_mul_f32 v[198:199], v[60:61], v[100:101] op_sel_hi:[1,0]
	v_pk_mul_f32 v[200:201], v[54:55], v[100:101] op_sel_hi:[1,0]
	v_pk_mul_f32 v[176:177], v[176:177], v[140:141]
	v_pk_mul_f32 v[140:141], v[102:103], v[142:143]
	v_pk_mul_f32 v[168:169], v[194:195], v[168:169]
	v_pk_mul_f32 v[142:143], v[192:193], v[138:139]
	v_pk_mul_f32 v[100:101], v[196:197], v[170:171]
	v_pk_mul_f32 v[138:139], v[202:203], v[172:173]
	v_cvt_pk_bf16_f32 v170, v176, v177
	v_cvt_pk_bf16_f32 v171, v140, v141
	v_cvt_pk_bf16_f32 v172, v168, v169
	v_cvt_pk_bf16_f32 v173, v142, v143
	v_pk_mul_f32 v[102:103], v[198:199], v[136:137]
	v_pk_mul_f32 v[136:137], v[200:201], v[174:175]
	global_store_dwordx4 v[188:189], v[170:173], off
	v_lshl_add_u64 v[174:175], s[24:25], 0, v[152:153]
	v_lshl_add_u64 v[174:175], v[174:175], 0, v[96:97]
	v_cvt_pk_bf16_f32 v170, v102, v103
	v_cvt_pk_bf16_f32 v171, v100, v101
	v_cvt_pk_bf16_f32 v172, v138, v139
	v_cvt_pk_bf16_f32 v173, v136, v137
	global_store_dwordx4 v[190:191], v[170:173], off
	s_nop 1
	v_lshl_add_u64 v[186:187], v[166:167], 0, v[96:97]
	v_max_f32_e64 v103, |v103|, |v139|
	v_pk_mul_f32 v[188:189], v[56:57], v[234:235] op_sel_hi:[1,0]
	v_pk_mul_f32 v[166:167], v[58:59], v[234:235] op_sel_hi:[1,0]
	v_pk_mul_f32 v[190:191], v[48:49], v[234:235] op_sel_hi:[1,0]
	v_pk_mul_f32 v[192:193], v[50:51], v[234:235] op_sel_hi:[1,0]
	v_pk_mul_f32 v[194:195], v[60:61], v[234:235] op_sel_hi:[1,0]
	v_pk_mul_f32 v[196:197], v[62:63], v[234:235] op_sel_hi:[1,0]
	v_pk_mul_f32 v[198:199], v[52:53], v[234:235] op_sel_hi:[1,0]
	v_pk_mul_f32 v[200:201], v[54:55], v[234:235] op_sel_hi:[1,0]
	v_pk_mul_f32 v[166:167], v[166:167], v[120:121]
	v_pk_mul_f32 v[120:121], v[188:189], v[122:123]
	v_pk_mul_f32 v[170:171], v[192:193], v[124:125]
	v_pk_mul_f32 v[126:127], v[190:191], v[126:127]
	v_pk_mul_f32 v[124:125], v[196:197], v[128:129]
	v_pk_mul_f32 v[122:123], v[194:195], v[130:131]
	v_pk_mul_f32 v[130:131], v[200:201], v[132:133]
	v_pk_mul_f32 v[128:129], v[198:199], v[134:135]
	v_cvt_pk_bf16_f32 v132, v120, v121
	v_cvt_pk_bf16_f32 v133, v166, v167
	v_cvt_pk_bf16_f32 v134, v126, v127
	v_cvt_pk_bf16_f32 v135, v170, v171
	global_store_dwordx4 v[186:187], v[132:135], off
	s_nop 1
	v_cvt_pk_bf16_f32 v132, v122, v123
	v_cvt_pk_bf16_f32 v133, v124, v125
	v_cvt_pk_bf16_f32 v134, v128, v129
	v_cvt_pk_bf16_f32 v135, v130, v131
	global_store_dwordx4 v[174:175], v[132:135], off
	s_nop 1
	v_lshlrev_b32_e32 v133, 8, v164
	v_and_b32_e32 v152, 0xfef00, v133
	v_lshl_add_u64 v[134:135], s[26:27], 0, v[152:153]
	v_lshl_add_u64 v[172:173], s[24:25], 0, v[152:153]
	v_lshl_add_u64 v[186:187], v[134:135], 0, v[96:97]
	v_lshl_add_u64 v[188:189], v[172:173], 0, v[96:97]
	v_pk_mul_f32 v[134:135], v[58:59], v[236:237] op_sel_hi:[1,0]
	v_pk_mul_f32 v[172:173], v[56:57], v[236:237] op_sel_hi:[1,0]
	v_pk_mul_f32 v[174:175], v[50:51], v[236:237] op_sel_hi:[1,0]
	v_pk_mul_f32 v[190:191], v[48:49], v[236:237] op_sel_hi:[1,0]
	v_pk_mul_f32 v[192:193], v[62:63], v[236:237] op_sel_hi:[1,0]
	v_pk_mul_f32 v[194:195], v[60:61], v[236:237] op_sel_hi:[1,0]
	v_pk_mul_f32 v[196:197], v[54:55], v[236:237] op_sel_hi:[1,0]
	v_pk_mul_f32 v[198:199], v[52:53], v[236:237] op_sel_hi:[1,0]
	v_pk_mul_f32 v[108:109], v[172:173], v[108:109]
	v_pk_mul_f32 v[104:105], v[134:135], v[104:105]
	v_pk_mul_f32 v[134:135], v[190:191], v[112:113]
	v_pk_mul_f32 v[132:133], v[174:175], v[106:107]
	v_cvt_pk_bf16_f32 v172, v108, v109
	v_cvt_pk_bf16_f32 v173, v104, v105
	v_cvt_pk_bf16_f32 v174, v134, v135
	v_pk_mul_f32 v[112:113], v[194:195], v[116:117]
	v_cvt_pk_bf16_f32 v175, v132, v133
	v_pk_mul_f32 v[106:107], v[192:193], v[110:111]
	v_pk_mul_f32 v[116:117], v[198:199], v[118:119]
	v_pk_mul_f32 v[110:111], v[196:197], v[114:115]
	global_store_dwordx4 v[186:187], v[172:175], off
	v_lshlrev_b32_e32 v115, 8, v162
	v_and_b32_e32 v152, 0xfff00, v115
	v_cvt_pk_bf16_f32 v172, v112, v113
	v_cvt_pk_bf16_f32 v173, v106, v107
	v_cvt_pk_bf16_f32 v174, v116, v117
	v_cvt_pk_bf16_f32 v175, v110, v111
	global_store_dwordx4 v[188:189], v[172:175], off
	s_nop 1
	v_lshl_add_u64 v[162:163], s[24:25], 0, v[152:153]
	v_lshl_add_u64 v[118:119], s[26:27], 0, v[152:153]
	v_lshl_add_u64 v[172:173], v[162:163], 0, v[96:97]
	v_lshl_add_u64 v[118:119], v[118:119], 0, v[96:97]
	v_lshlrev_b32_e32 v152, 8, v179
	v_and_b32_e32 v152, 0xfcf00, v152
	v_pk_mul_f32 v[162:163], v[56:57], v[238:239] op_sel_hi:[1,0]
	v_pk_mul_f32 v[164:165], v[58:59], v[238:239] op_sel_hi:[1,0]
	v_pk_mul_f32 v[174:175], v[48:49], v[238:239] op_sel_hi:[1,0]
	v_pk_mul_f32 v[186:187], v[50:51], v[238:239] op_sel_hi:[1,0]
	v_pk_mul_f32 v[188:189], v[60:61], v[238:239] op_sel_hi:[1,0]
	v_pk_mul_f32 v[190:191], v[62:63], v[238:239] op_sel_hi:[1,0]
	v_pk_mul_f32 v[192:193], v[52:53], v[238:239] op_sel_hi:[1,0]
	v_pk_mul_f32 v[194:195], v[54:55], v[238:239] op_sel_hi:[1,0]
	v_pk_mul_f32 v[114:115], v[164:165], v[88:89]
	v_pk_mul_f32 v[88:89], v[162:163], v[90:91]
	v_pk_mul_f32 v[92:93], v[186:187], v[92:93]
	v_pk_mul_f32 v[90:91], v[174:175], v[94:95]
	v_cvt_pk_bf16_f32 v162, v88, v89
	v_cvt_pk_bf16_f32 v163, v114, v115
	v_pk_mul_f32 v[86:87], v[190:191], v[86:87]
	v_cvt_pk_bf16_f32 v164, v90, v91
	v_cvt_pk_bf16_f32 v165, v92, v93
	v_pk_mul_f32 v[84:85], v[188:189], v[84:85]
	v_pk_mul_f32 v[82:83], v[194:195], v[82:83]
	v_pk_mul_f32 v[80:81], v[192:193], v[80:81]
	global_store_dwordx4 v[118:119], v[162:165], off
	v_ashrrev_i32_e32 v94, 8, v179
	v_and_b32_e32 v94, -16, v94
	v_cvt_pk_bf16_f32 v162, v84, v85
	v_cvt_pk_bf16_f32 v163, v86, v87
	v_cvt_pk_bf16_f32 v164, v80, v81
	v_cvt_pk_bf16_f32 v165, v82, v83
	global_store_dwordx4 v[172:173], v[162:165], off
	s_nop 1
	v_add_u32_e32 v94, s17, v94
	v_or_b32_e32 v118, 1, v94
	v_ashrrev_i32_e32 v119, 31, v118
	v_ashrrev_i32_e32 v95, 31, v94
	v_lshlrev_b64 v[118:119], 20, v[118:119]
	v_lshlrev_b64 v[94:95], 20, v[94:95]
	v_lshl_add_u64 v[118:119], s[6:7], 0, v[118:119]
	v_lshl_add_u64 v[94:95], s[6:7], 0, v[94:95]
	v_lshl_add_u64 v[172:173], v[118:119], 0, v[152:153]
	v_lshl_add_u64 v[164:165], v[94:95], 0, v[152:153]
	v_lshl_add_u64 v[186:187], v[172:173], 0, v[96:97]
	v_lshl_add_u64 v[164:165], v[164:165], 0, v[96:97]
	v_max_f32_e64 v88, |v88|, |v90|
	v_max_f32_e64 v82, |v86|, |v82|
	v_max_f32_e64 v83, |v87|, |v83|
	v_max_f32_e64 v80, |v84|, |v80|
	v_max_f32_e64 v89, |v89|, |v91|
	v_max_f32_e64 v81, |v85|, |v81|
	v_pk_mul_f32 v[172:173], v[58:59], v[240:241] op_sel_hi:[1,0]
	v_pk_mul_f32 v[174:175], v[56:57], v[240:241] op_sel_hi:[1,0]
	v_pk_mul_f32 v[188:189], v[50:51], v[240:241] op_sel_hi:[1,0]
	v_pk_mul_f32 v[190:191], v[48:49], v[240:241] op_sel_hi:[1,0]
	v_pk_mul_f32 v[192:193], v[62:63], v[240:241] op_sel_hi:[1,0]
	v_pk_mul_f32 v[194:195], v[60:61], v[240:241] op_sel_hi:[1,0]
	v_pk_mul_f32 v[196:197], v[54:55], v[240:241] op_sel_hi:[1,0]
	v_pk_mul_f32 v[198:199], v[52:53], v[240:241] op_sel_hi:[1,0]
	v_pk_mul_f32 v[162:163], v[174:175], v[76:77]
	v_pk_mul_f32 v[76:77], v[172:173], v[78:79]
	v_pk_mul_f32 v[78:79], v[190:191], v[72:73]
	v_pk_mul_f32 v[74:75], v[188:189], v[74:75]
	v_cvt_pk_bf16_f32 v172, v162, v163
	v_cvt_pk_bf16_f32 v173, v76, v77
	v_cvt_pk_bf16_f32 v174, v78, v79
	v_pk_mul_f32 v[72:73], v[194:195], v[68:69]
	v_cvt_pk_bf16_f32 v175, v74, v75
	v_pk_mul_f32 v[68:69], v[192:193], v[70:71]
	v_pk_mul_f32 v[70:71], v[198:199], v[64:65]
	v_pk_mul_f32 v[64:65], v[196:197], v[66:67]
	global_store_dwordx4 v[164:165], v[172:175], off
	v_cvt_f32_i32_e32 v165, v37
	v_cvt_f32_i32_e32 v164, v36
	v_cvt_pk_bf16_f32 v172, v72, v73
	v_cvt_pk_bf16_f32 v173, v68, v69
	v_cvt_pk_bf16_f32 v174, v70, v71
	v_cvt_pk_bf16_f32 v175, v64, v65
	global_store_dwordx4 v[186:187], v[172:175], off
	s_nop 1
	v_max_f32_e64 v78, |v162|, |v78|
	v_cvt_f32_i32_e32 v173, v33
	v_cvt_f32_i32_e32 v172, v32
	v_cvt_f32_i32_e32 v175, v35
	v_cvt_f32_i32_e32 v174, v34
	v_add_u32_e32 v32, 0x9000, v178
	v_and_b32_e32 v152, 0xfdf00, v32
	v_lshl_add_u64 v[32:33], v[94:95], 0, v[152:153]
	v_lshl_add_u64 v[34:35], v[118:119], 0, v[152:153]
	v_lshl_add_u64 v[186:187], v[32:33], 0, v[96:97]
	v_lshl_add_u64 v[188:189], v[34:35], 0, v[96:97]
	v_add_u32_e32 v152, 0xa000, v178
	v_and_b32_e32 v152, 0xfef00, v152
	v_max_f32_e64 v75, |v77|, |v75|
	v_max_f32_e64 v74, |v76|, |v74|
	v_max_f32_e64 v70, |v72|, |v70|
	v_max_f32_e64 v65, |v69|, |v65|
	v_max_f32_e64 v64, |v68|, |v64|
	v_max_f32_e64 v71, |v73|, |v71|
	v_pk_mul_f32 v[32:33], v[58:59], v[242:243] op_sel_hi:[1,0]
	v_pk_mul_f32 v[34:35], v[56:57], v[242:243] op_sel_hi:[1,0]
	v_pk_mul_f32 v[190:191], v[50:51], v[242:243] op_sel_hi:[1,0]
	v_pk_mul_f32 v[192:193], v[48:49], v[242:243] op_sel_hi:[1,0]
	v_pk_mul_f32 v[194:195], v[62:63], v[242:243] op_sel_hi:[1,0]
	v_pk_mul_f32 v[196:197], v[60:61], v[242:243] op_sel_hi:[1,0]
	v_pk_mul_f32 v[198:199], v[54:55], v[242:243] op_sel_hi:[1,0]
	v_pk_mul_f32 v[66:67], v[52:53], v[242:243] op_sel_hi:[1,0]
	v_pk_mul_f32 v[36:37], v[32:33], v[46:47]
	v_pk_mul_f32 v[32:33], v[34:35], v[44:45]
	v_pk_mul_f32 v[44:45], v[190:191], v[42:43]
	v_pk_mul_f32 v[40:41], v[192:193], v[40:41]
	v_pk_mul_f32 v[46:47], v[198:199], v[174:175]
	v_pk_mul_f32 v[42:43], v[66:67], v[172:173]
	v_cvt_pk_bf16_f32 v172, v32, v33
	v_cvt_pk_bf16_f32 v173, v36, v37
	v_cvt_pk_bf16_f32 v174, v40, v41
	v_cvt_pk_bf16_f32 v175, v44, v45
	v_pk_mul_f32 v[38:39], v[194:195], v[38:39]
	v_pk_mul_f32 v[34:35], v[196:197], v[164:165]
	global_store_dwordx4 v[186:187], v[172:175], off
	v_cvt_f32_i32_e32 v164, v0
	v_and_b32_e32 v0, 64, v184
	v_cvt_pk_bf16_f32 v172, v34, v35
	v_cvt_pk_bf16_f32 v173, v38, v39
	v_cvt_pk_bf16_f32 v174, v42, v43
	v_cvt_pk_bf16_f32 v175, v46, v47
	global_store_dwordx4 v[188:189], v[172:175], off
	s_nop 1
	v_cvt_f32_i32_e32 v165, v1
	v_xor_b32_e32 v1, 1, v184
	v_add_u32_e32 v190, 64, v0
	v_cvt_f32_i32_e32 v172, v2
	v_xor_b32_e32 v2, 2, v184
	v_cmp_lt_i32_e32 vcc, v1, v190
	v_cvt_f32_i32_e32 v173, v3
	v_xor_b32_e32 v3, 4, v184
	v_cndmask_b32_e32 v0, v184, v1, vcc
	v_cmp_lt_i32_e32 vcc, v2, v190
	v_xor_b32_e32 v67, 8, v184
	v_lshlrev_b32_e32 v194, 2, v0
	v_cndmask_b32_e32 v191, v184, v2, vcc
	v_cmp_lt_i32_e32 vcc, v3, v190
	v_lshl_add_u64 v[0:1], v[94:95], 0, v[152:153]
	v_add_u32_e32 v189, 0xb000, v178
	v_cndmask_b32_e32 v192, v184, v3, vcc
	v_lshl_add_u64 v[2:3], v[118:119], 0, v[152:153]
	v_cmp_lt_i32_e32 vcc, v67, v190
	v_lshl_add_u64 v[174:175], v[0:1], 0, v[96:97]
	v_lshl_add_u64 v[178:179], v[2:3], 0, v[96:97]
	v_max_f32_e64 v196, |v141|, |v143|
	v_max_f32_e64 v197, |v140|, |v142|
	v_cndmask_b32_e32 v193, v184, v67, vcc
	v_max_f32_e64 v152, |v177|, |v169|
	v_max_f32_e64 v195, |v176|, |v168|
	v_max_f32_e64 v36, |v36|, |v44|
	v_max_f32_e64 v37, |v37|, |v45|
	v_max_f32_e64 v32, |v32|, |v40|
	v_max_f32_e64 v38, |v38|, |v46|
	v_max_f32_e64 v39, |v39|, |v47|
	v_max_f32_e64 v34, |v34|, |v42|
	v_max_f32_e64 v33, |v33|, |v41|
	v_max_f32_e64 v35, |v35|, |v43|
	v_cmp_lt_i32_e32 vcc, v185, v190
	v_xor_b32_e32 v188, 32, v184
	v_pk_mul_f32 v[0:1], v[58:59], v[244:245] op_sel_hi:[1,0]
	v_pk_mul_f32 v[2:3], v[56:57], v[244:245] op_sel_hi:[1,0]
	v_pk_mul_f32 v[140:141], v[50:51], v[244:245] op_sel_hi:[1,0]
	v_pk_mul_f32 v[142:143], v[48:49], v[244:245] op_sel_hi:[1,0]
	v_pk_mul_f32 v[168:169], v[62:63], v[244:245] op_sel_hi:[1,0]
	v_pk_mul_f32 v[176:177], v[60:61], v[244:245] op_sel_hi:[1,0]
	v_pk_mul_f32 v[186:187], v[54:55], v[244:245] op_sel_hi:[1,0]
	v_pk_mul_f32 v[66:67], v[52:53], v[244:245] op_sel_hi:[1,0]
	v_pk_mul_f32 v[28:29], v[2:3], v[28:29]
	v_pk_mul_f32 v[30:31], v[0:1], v[30:31]
	v_pk_mul_f32 v[24:25], v[142:143], v[24:25]
	v_pk_mul_f32 v[26:27], v[140:141], v[26:27]
	v_cvt_pk_bf16_f32 v0, v28, v29
	v_cvt_pk_bf16_f32 v1, v30, v31
	v_cvt_pk_bf16_f32 v2, v24, v25
	v_pk_mul_f32 v[20:21], v[176:177], v[20:21]
	v_cvt_pk_bf16_f32 v3, v26, v27
	v_pk_mul_f32 v[22:23], v[168:169], v[22:23]
	v_pk_mul_f32 v[16:17], v[66:67], v[16:17]
	v_pk_mul_f32 v[18:19], v[186:187], v[18:19]
	global_store_dwordx4 v[174:175], v[0:3], off
	v_max3_f32 v66, v152, 0, v103
	v_max_f32_e64 v67, |v166|, |v170|
	v_cvt_pk_bf16_f32 v0, v20, v21
	v_cvt_pk_bf16_f32 v1, v22, v23
	v_cvt_pk_bf16_f32 v2, v16, v17
	v_cvt_pk_bf16_f32 v3, v18, v19
	global_store_dwordx4 v[178:179], v[0:3], off
	s_nop 1
	v_max_f32_e64 v98, |v167|, |v171|
	v_max_f32_e64 v1, |v102|, |v138|
	v_max_f32_e64 v2, |v101|, |v137|
	v_max_f32_e64 v3, |v100|, |v136|
	v_max3_f32 v3, v197, 0, v3
	v_max3_f32 v2, v196, 0, v2
	v_max3_f32 v1, v195, 0, v1
	v_max_f32_e64 v99, |v120|, |v126|
	v_max_f32_e64 v100, |v121|, |v127|
	v_max_f32_e64 v101, |v124|, |v130|
	v_max_f32_e64 v102, |v125|, |v131|
	v_max_f32_e64 v103, |v122|, |v128|
	v_max_f32_e64 v120, |v123|, |v129|
	v_max3_f32 v66, v66, v100, v120
	v_max3_f32 v1, v1, v99, v103
	v_max3_f32 v2, v2, v98, v102
	v_max3_f32 v3, v3, v67, v101
	v_max_f32_e64 v67, |v109|, |v135|
	v_max_f32_e64 v98, |v108|, |v134|
	v_max_f32_e64 v99, |v105|, |v133|
	v_max_f32_e64 v100, |v104|, |v132|
	v_max_f32_e64 v101, |v113|, |v117|
	v_max_f32_e64 v102, |v112|, |v116|
	v_max_f32_e64 v103, |v107|, |v111|
	v_max_f32_e64 v104, |v106|, |v110|
	v_max3_f32 v3, v3, v100, v104
	v_max3_f32 v2, v2, v99, v103
	v_max3_f32 v1, v1, v98, v102
	v_max3_f32 v66, v66, v67, v101
	v_max_f32_e64 v67, |v114|, |v92|
	v_max_f32_e64 v92, |v115|, |v93|
	v_max3_f32 v1, v1, v88, v80
	v_max3_f32 v2, v2, v92, v83
	v_max3_f32 v3, v3, v67, v82
	v_max3_f32 v66, v66, v89, v81
	v_max_f32_e64 v67, |v163|, |v79|
	v_max3_f32 v3, v3, v74, v64
	v_max3_f32 v2, v2, v75, v65
	v_max3_f32 v1, v1, v78, v70
	v_max3_f32 v64, v66, v67, v71
	v_max3_f32 v1, v1, v32, v34
	v_max3_f32 v2, v2, v37, v39
	v_max3_f32 v3, v3, v36, v38
	v_max_f32_e64 v27, |v31|, |v27|
	v_max_f32_e64 v26, |v30|, |v26|
	v_max_f32_e64 v19, |v23|, |v19|
	v_max_f32_e64 v18, |v22|, |v18|
	v_max3_f32 v33, v64, v33, v35
	v_max_f32_e64 v25, |v29|, |v25|
	v_max_f32_e64 v24, |v28|, |v24|
	v_max_f32_e64 v17, |v21|, |v17|
	v_max_f32_e64 v16, |v20|, |v16|
	v_max3_f32 v28, v3, v26, v18
	v_max3_f32 v29, v2, v27, v19
	v_max3_f32 v30, v1, v24, v16
	v_max3_f32 v31, v33, v25, v17
	v_and_b32_e32 v152, 0xfff00, v189
	v_pk_mul_f32 v[2:3], v[58:59], v[246:247] op_sel_hi:[1,0]
	v_pk_mul_f32 v[18:19], v[50:51], v[246:247] op_sel_hi:[1,0]
	v_pk_mul_f32 v[22:23], v[62:63], v[246:247] op_sel_hi:[1,0]
	v_pk_mul_f32 v[26:27], v[54:55], v[246:247] op_sel_hi:[1,0]
	v_pk_mul_f32 v[16:17], v[56:57], v[246:247] op_sel_hi:[1,0]
	v_pk_mul_f32 v[20:21], v[48:49], v[246:247] op_sel_hi:[1,0]
	v_pk_mul_f32 v[24:25], v[60:61], v[246:247] op_sel_hi:[1,0]
	v_pk_mul_f32 v[0:1], v[52:53], v[246:247] op_sel_hi:[1,0]
	v_pk_mul_f32 v[2:3], v[2:3], v[14:15]
	v_pk_mul_f32 v[10:11], v[18:19], v[10:11]
	v_pk_mul_f32 v[6:7], v[22:23], v[6:7]
	v_pk_mul_f32 v[14:15], v[26:27], v[172:173]
	v_pk_mul_f32 v[12:13], v[16:17], v[12:13]
	v_pk_mul_f32 v[8:9], v[20:21], v[8:9]
	v_pk_mul_f32 v[4:5], v[24:25], v[4:5]
	v_pk_mul_f32 v[16:17], v[0:1], v[164:165]
	v_max_f32_e64 v0, |v2|, |v10|
	v_max_f32_e64 v1, |v3|, |v11|
	v_max_f32_e64 v20, |v6|, |v14|
	v_max_f32_e64 v21, |v7|, |v15|
	v_max_f32_e64 v18, |v12|, |v8|
	v_max_f32_e64 v19, |v13|, |v9|
	v_max_f32_e64 v22, |v4|, |v16|
	v_max_f32_e64 v23, |v5|, |v17|
	v_max3_f32 v1, v29, v1, v21
	v_max3_f32 v0, v28, v0, v20
	v_max3_f32 v19, v31, v19, v23
	v_max3_f32 v18, v30, v18, v22
	v_max_f32_e32 v0, v0, v1
	v_max3_f32 v0, v18, v19, v0
	ds_bpermute_b32 v1, v194, v0
	v_lshlrev_b32_e32 v19, 2, v191
	v_lshlrev_b32_e32 v23, 2, v193
	v_cndmask_b32_e32 v18, v184, v185, vcc
	v_lshlrev_b32_e32 v24, 2, v18
	s_waitcnt lgkmcnt(0)
	v_max_f32_e32 v1, v1, v1
	v_max_f32_e32 v0, v0, v1
	ds_bpermute_b32 v1, v19, v0
	v_lshlrev_b32_e32 v19, 2, v192
	v_cmp_lt_i32_e32 vcc, v188, v190
	s_waitcnt lgkmcnt(0)
	v_max_f32_e32 v1, v1, v1
	v_max_f32_e32 v25, v0, v1
	ds_bpermute_b32 v26, v19, v25
	v_lshl_add_u64 v[0:1], v[94:95], 0, v[152:153]
	v_lshl_add_u64 v[20:21], v[0:1], 0, v[96:97]
	v_cvt_pk_bf16_f32 v0, v12, v13
	v_cndmask_b32_e32 v22, v184, v188, vcc
	s_waitcnt lgkmcnt(0)
	v_max_f32_e32 v1, v26, v26
	v_max_f32_e32 v12, v25, v1
	ds_bpermute_b32 v13, v23, v12
	v_cvt_pk_bf16_f32 v1, v2, v3
	v_cvt_pk_bf16_f32 v2, v8, v9
	v_cvt_pk_bf16_f32 v3, v10, v11
	global_store_dwordx4 v[20:21], v[0:3], off
	v_lshl_add_u64 v[18:19], v[118:119], 0, v[152:153]
	s_waitcnt lgkmcnt(0)
	v_max_f32_e32 v0, v13, v13
	v_max_f32_e32 v0, v12, v0
	ds_bpermute_b32 v1, v24, v0
	v_cvt_pk_bf16_f32 v2, v4, v5
	v_cvt_pk_bf16_f32 v3, v6, v7
	v_lshl_add_u64 v[6:7], v[18:19], 0, v[96:97]
	v_cvt_pk_bf16_f32 v4, v16, v17
	s_waitcnt lgkmcnt(0)
	v_max_f32_e32 v1, v1, v1
	v_max_f32_e32 v0, v0, v1
	v_lshlrev_b32_e32 v1, 2, v22
	ds_bpermute_b32 v1, v1, v0
	v_cvt_pk_bf16_f32 v5, v14, v15
	global_store_dwordx4 v[6:7], v[2:5], off
	s_nop 1
	v_mbcnt_lo_u32_b32 v2, -1, 0
	v_mbcnt_hi_u32_b32 v2, -1, v2
	s_nop 0
	v_cmp_eq_u32_e32 vcc, 0, v2
	s_and_saveexec_b64 s[24:25], vcc
	s_cbranch_execz .LBB0_718
	s_waitcnt lgkmcnt(0)
	v_max_f32_e32 v1, v1, v1
	v_max_f32_e32 v0, v0, v0
	s_mov_b64 s[26:27], exec
	v_max_f32_e32 v0, v0, v1
	s_mov_b32 s17, 0
